# more nt streaming hints: converted-weight stores, P6 X1 row loads, dense attention Q loads
# speedup vs baseline: 1.0064x; 1.0033x over previous
.LBB0_248:
	v_cmp_eq_u32_e32 vcc, 0, v155
	v_add3_u32 v155, s65, v138, v139
	v_add3_u32 v160, s65, v140, v141
	s_ashr_i32 s42, s67, 31
	ds_read_b128 v[156:159], v155
	ds_read_b128 v[160:163], v160
	v_add3_u32 v155, s65, v142, v143
	v_add3_u32 v168, s65, v144, v145
	s_add_u32 s6, s6, s67
	ds_read_b128 v[164:167], v155
	ds_read_b128 v[168:171], v168
	s_addc_u32 s7, s7, s42
	s_cmpk_gt_i32 s66, 0x7ff
	v_lshl_add_u64 v[172:173], s[6:7], 0, v[2:3]
	s_cselect_b64 s[6:7], -1, 0
	s_and_b64 s[58:59], s[6:7], exec
	v_add_u32_e32 v0, s66, v135
	s_cselect_b32 s42, 0x80, 0
	v_add_u32_e32 v155, 0xfffff800, v0
	v_cndmask_b32_e64 v155, v0, v155, s[6:7]
	v_lshlrev_b32_e32 v174, 1, v155
	v_and_b32_e32 v174, 0xffffff00, v174
	v_and_b32_e32 v155, 0x7f, v155
	v_or3_b32 v155, v155, v174, s42
	v_cndmask_b32_e32 v174, v155, v0, vcc
	v_ashrrev_i32_e32 v175, 31, v174
	v_lshlrev_b64 v[174:175], 11, v[174:175]
	v_lshl_add_u64 v[174:175], v[172:173], 0, v[174:175]
	s_waitcnt lgkmcnt(3)
	global_store_dwordx4 v[174:175], v[156:159], off nt
	v_add_u32_e32 v155, 4, v0
	s_nop 0
	v_add_u32_e32 v156, 0xfffff804, v0
	v_cndmask_b32_e64 v156, v155, v156, s[6:7]
	v_lshlrev_b32_e32 v157, 1, v156
	v_and_b32_e32 v157, 0xffffff00, v157
	v_and_b32_e32 v156, 0x7f, v156
	v_or3_b32 v156, v156, v157, s42
	v_cndmask_b32_e32 v156, v156, v155, vcc
	v_ashrrev_i32_e32 v157, 31, v156
	v_lshlrev_b64 v[156:157], 11, v[156:157]
	v_lshl_add_u64 v[156:157], v[172:173], 0, v[156:157]
	s_waitcnt lgkmcnt(2)
	global_store_dwordx4 v[156:157], v[160:163], off nt
	v_add_u32_e32 v155, 8, v0
	v_add_u32_e32 v156, 0xfffff808, v0
	v_cndmask_b32_e64 v156, v155, v156, s[6:7]
	v_lshlrev_b32_e32 v157, 1, v156
	v_and_b32_e32 v157, 0xffffff00, v157
	v_and_b32_e32 v156, 0x7f, v156
	v_or3_b32 v156, v156, v157, s42
	v_cndmask_b32_e32 v156, v156, v155, vcc
	v_ashrrev_i32_e32 v157, 31, v156
	v_lshlrev_b64 v[156:157], 11, v[156:157]
	v_lshl_add_u64 v[156:157], v[172:173], 0, v[156:157]
	s_waitcnt lgkmcnt(1)
	global_store_dwordx4 v[156:157], v[164:167], off nt
	v_add_u32_e32 v155, 12, v0
	v_add_u32_e32 v156, 0xfffff80c, v0
	v_cndmask_b32_e64 v156, v155, v156, s[6:7]
	v_lshlrev_b32_e32 v157, 1, v156
	v_and_b32_e32 v157, 0xffffff00, v157
	v_and_b32_e32 v156, 0x7f, v156
	v_or3_b32 v156, v156, v157, s42
	v_cndmask_b32_e32 v156, v156, v155, vcc
	v_ashrrev_i32_e32 v157, 31, v156
	v_lshlrev_b64 v[156:157], 11, v[156:157]
	v_lshl_add_u64 v[156:157], v[172:173], 0, v[156:157]
	v_add3_u32 v155, s65, v146, v147
	s_waitcnt lgkmcnt(0)
	global_store_dwordx4 v[156:157], v[168:171], off nt
	ds_read_b128 v[156:159], v155
	v_add3_u32 v155, s65, v148, v149
	ds_read_b128 v[160:163], v155
	v_add3_u32 v155, s65, v150, v151
	ds_read_b128 v[164:167], v155
	v_add3_u32 v155, s65, v152, v153
	ds_read_b128 v[168:171], v155
	v_add_u32_e32 v155, 16, v0
	v_add_u32_e32 v174, 0xfffff810, v0
	v_cndmask_b32_e64 v174, v155, v174, s[6:7]
	v_lshlrev_b32_e32 v175, 1, v174
	v_and_b32_e32 v175, 0xffffff00, v175
	v_and_b32_e32 v174, 0x7f, v174
	v_or3_b32 v174, v174, v175, s42
	v_cndmask_b32_e32 v174, v174, v155, vcc
	v_ashrrev_i32_e32 v175, 31, v174
	v_lshlrev_b64 v[174:175], 11, v[174:175]
	v_lshl_add_u64 v[174:175], v[172:173], 0, v[174:175]
	s_waitcnt lgkmcnt(3)
	global_store_dwordx4 v[174:175], v[156:159], off nt
	v_add_u32_e32 v155, 20, v0
	s_xor_b32 s62, s62, 1
	v_add_u32_e32 v156, 0xfffff814, v0
	v_cndmask_b32_e64 v156, v155, v156, s[6:7]
	v_lshlrev_b32_e32 v157, 1, v156
	v_and_b32_e32 v157, 0xffffff00, v157
	v_and_b32_e32 v156, 0x7f, v156
	v_or3_b32 v156, v156, v157, s42
	v_cndmask_b32_e32 v156, v156, v155, vcc
	v_ashrrev_i32_e32 v157, 31, v156
	v_lshlrev_b64 v[156:157], 11, v[156:157]
	v_lshl_add_u64 v[156:157], v[172:173], 0, v[156:157]
	s_waitcnt lgkmcnt(2)
	global_store_dwordx4 v[156:157], v[160:163], off nt
	v_add_u32_e32 v155, 24, v0
	v_add_u32_e32 v156, 0xfffff818, v0
	v_cndmask_b32_e64 v156, v155, v156, s[6:7]
	v_lshlrev_b32_e32 v157, 1, v156
	v_and_b32_e32 v157, 0xffffff00, v157
	v_and_b32_e32 v156, 0x7f, v156
	v_or3_b32 v156, v156, v157, s42
	v_cndmask_b32_e32 v156, v156, v155, vcc
	v_ashrrev_i32_e32 v157, 31, v156
	v_lshlrev_b64 v[156:157], 11, v[156:157]
	v_add_u32_e32 v155, 28, v0
	v_add_u32_e32 v0, 0xfffff81c, v0
	v_lshl_add_u64 v[156:157], v[172:173], 0, v[156:157]
	v_cndmask_b32_e64 v0, v155, v0, s[6:7]
	s_waitcnt lgkmcnt(1)
	global_store_dwordx4 v[156:157], v[164:167], off nt
	v_lshlrev_b32_e32 v156, 1, v0
	v_and_b32_e32 v156, 0xffffff00, v156
	v_and_b32_e32 v0, 0x7f, v0
	v_or3_b32 v0, v0, v156, s42
	v_cndmask_b32_e32 v156, v0, v155, vcc
	v_ashrrev_i32_e32 v157, 31, v156
	v_lshlrev_b64 v[156:157], 11, v[156:157]
	v_lshl_add_u64 v[156:157], v[172:173], 0, v[156:157]
	s_add_i32 s10, s10, s11
	s_add_i32 s44, s44, s53
	s_andn2_b64 vcc, exec, s[54:55]
	s_mov_b64 s[6:7], s[14:15]
	s_mov_b32 s67, s64
	s_mov_b32 s66, s56
	v_mov_b32_e32 v155, v154
	s_waitcnt lgkmcnt(0)
	global_store_dwordx4 v[156:157], v[168:171], off nt
	s_cbranch_vccz .LBB0_254

.LBB0_334:
	s_and_b64 vcc, exec, s[60:61]
	s_cbranch_vccz .LBB0_242
	v_readlane_b32 s10, v254, 20
	s_add_u32 s10, s10, s56
	v_readlane_b32 s11, v254, 19
	s_addc_u32 s11, s11, s57
	s_add_u32 s14, s10, s58
	s_addc_u32 s15, s11, s59
	s_lshl_b64 s[90:91], s[54:55], 1
	s_add_u32 s10, s73, s90
	v_readfirstlane_b32 s11, v235
	s_addc_u32 s44, s75, s91
	s_lshr_b32 s42, s11, 6
	s_lshl_b32 s53, s42, 5
	s_mul_i32 s54, s42, 0xc000
	s_mul_hi_u32 s55, s53, 0x600
	s_lshl_b64 vcc, s[54:55], 1
	s_add_u32 s62, s10, vcc_lo
	s_addc_u32 s63, s44, vcc_hi
	s_lshl_b32 s10, s42, 4
	v_add_u32_e32 v165, s10, v208
	v_and_or_b32 v0, s10, 48, v201
	s_lshr_b32 s10, s11, 3
	s_and_b32 s10, s10, 0x1fffffe0
	s_lshl_b32 s44, s42, 10
	v_mov_b32_e32 v2, s10
	s_movk_i32 s10, 0x180
	s_cmp_lg_u32 0, -1
	v_mad_u32_u24 v0, v0, s10, v2
	s_cselect_b32 s10, 0, 0
	s_add_i32 s70, s44, s10
	v_or_b32_e32 v0, v0, v209
	s_add_i32 s10, s70, 0xc000
	s_mov_b32 m0, s70
	s_nop 0
	global_load_lds_dwordx4 v165, s[88:89]
	v_lshlrev_b32_e32 v164, 1, v0
	s_mov_b32 m0, s10
	s_nop 0
	global_load_lds_dwordx4 v164, s[14:15]
	s_add_u32 s54, s88, 0xc000
	s_addc_u32 s55, s89, 0
	s_add_i32 s71, s70, 0x2000
	s_mov_b32 m0, s71
	s_nop 0
	global_load_lds_dwordx4 v165, s[54:55]
	global_load_dwordx4 v[140:143], v217, s[62:63] nt
	global_load_dwordx4 v[128:131], v217, s[62:63] offset:32 nt
	global_load_dwordx4 v[136:139], v217, s[62:63] offset:64 nt
	global_load_dwordx4 v[132:135], v217, s[62:63] offset:96 nt
	s_add_u32 s64, s88, 0x18000
	s_addc_u32 s65, s89, 0
	s_add_i32 s76, s70, 0x4000
	s_add_u32 s62, s88, 0x24000
	s_mov_b32 m0, s76
	s_nop 0
	global_load_lds_dwordx4 v165, s[64:65]
	s_addc_u32 s63, s89, 0
	s_add_i32 s77, s70, 0x6000
	s_mov_b32 m0, s77
	s_nop 0
	global_load_lds_dwordx4 v165, s[62:63]
	s_add_u32 s62, s14, 0xc000
	s_addc_u32 s63, s15, 0
	s_add_i32 s78, s70, 0xe000
	s_mov_b32 m0, s78
	s_nop 0
	global_load_lds_dwordx4 v164, s[62:63]
	s_add_u32 s62, s88, 0x30000
	s_addc_u32 s63, s89, 0
	s_add_i32 s79, s70, 0x8000
	s_mov_b32 m0, s79
	s_nop 0
	global_load_lds_dwordx4 v165, s[62:63]
	s_add_u32 s62, s88, 0x3c000
	s_addc_u32 s63, s89, 0
	s_add_i32 s85, s70, 0xa000
	s_mov_b32 m0, s85
	s_nop 0
	global_load_lds_dwordx4 v165, s[62:63]
	s_add_u32 s62, s14, 0x18000
	s_addc_u32 s63, s15, 0
	s_add_i32 s92, s70, 0x10000
	s_mov_b32 m0, s92
	s_nop 0
	global_load_lds_dwordx4 v164, s[62:63]
	s_add_u32 s62, s14, 0x24000
	s_addc_u32 s63, s15, 0
	s_add_i32 s93, s70, 0x12000
	s_mov_b32 m0, s93
	s_nop 0
	global_load_lds_dwordx4 v164, s[62:63]
	s_waitcnt vmcnt(7) lgkmcnt(0)
	s_barrier
	s_waitcnt vmcnt(22)
	ds_read_b128 v[36:39], v210
	s_waitcnt vmcnt(21)
	ds_read_b128 v[40:43], v210 offset:512
	s_mov_b32 s53, s52
	s_mov_b32 s54, s52
	s_mov_b32 s55, s52
	s_mov_b32 s56, s52
	s_mov_b32 s57, s52
	s_mov_b32 s58, s52
	s_mov_b32 s59, s52
	s_mov_b32 s60, s52
	s_mov_b32 s61, s52
	s_mov_b32 s62, s52
	s_mov_b32 s63, s52
	s_mov_b32 s64, s52
	s_mov_b32 s65, s52
	s_mov_b32 s66, s52
	s_mov_b32 s67, s52
	s_waitcnt vmcnt(13)
	v_mov_b64_e32 v[4:5], s[52:53]
	v_mov_b64_e32 v[6:7], s[54:55]
	v_mov_b64_e32 v[8:9], s[56:57]
	v_mov_b64_e32 v[10:11], s[58:59]
	v_mov_b64_e32 v[12:13], s[60:61]
	v_mov_b64_e32 v[14:15], s[62:63]
	v_mov_b64_e32 v[16:17], s[64:65]
	v_mov_b64_e32 v[18:19], s[66:67]
	v_mov_b32_e32 v148, 0
	v_mov_b32_e32 v2, 0
	v_mov_b32_e32 v72, 0
	s_mov_b32 s53, -5
	s_waitcnt lgkmcnt(1)
	v_mfma_f32_32x32x16_bf16 v[20:35], v[36:39], v[140:143], v[4:19]
	s_mov_b64 s[54:55], 0
	v_mov_b32_e32 v73, 0
	v_mov_b32_e32 v149, v148
	v_mov_b32_e32 v150, v148
	v_mov_b32_e32 v151, v148
	s_waitcnt lgkmcnt(0)
	v_mfma_f32_32x32x16_bf16 v[4:19], v[40:43], v[140:143], v[4:19]
	ds_read_b128 v[36:39], v210 offset:2048
	ds_read_b128 v[40:43], v210 offset:2560
	s_waitcnt lgkmcnt(1)
	v_mfma_f32_32x32x16_bf16 v[20:35], v[36:39], v[128:131], v[20:35]
	s_waitcnt lgkmcnt(0)
	v_mfma_f32_32x32x16_bf16 v[4:19], v[40:43], v[128:131], v[4:19]
	ds_read_b128 v[36:39], v210 offset:4096
	ds_read_b128 v[40:43], v210 offset:4608
	s_waitcnt lgkmcnt(1)
	v_mfma_f32_32x32x16_bf16 v[20:35], v[36:39], v[136:139], v[20:35]
	s_waitcnt lgkmcnt(0)
	v_mfma_f32_32x32x16_bf16 v[4:19], v[40:43], v[136:139], v[4:19]
	ds_read_b128 v[36:39], v210 offset:6144
	ds_read_b128 v[40:43], v210 offset:6656
	s_waitcnt lgkmcnt(1)
	v_mfma_f32_32x32x16_bf16 v[20:35], v[36:39], v[132:135], v[20:35]
	s_waitcnt lgkmcnt(0)
	v_mfma_f32_32x32x16_bf16 v[4:19], v[40:43], v[132:135], v[4:19]
	s_nop 15
	s_nop 7
	s_waitcnt vmcnt(4) lgkmcnt(0)
	s_barrier
	ds_read_b128 v[68:71], v210 offset:8192
	ds_read_b128 v[160:163], v210 offset:8704
	ds_read_b128 v[156:159], v210 offset:10240
	ds_read_b128 v[112:115], v210 offset:10752
	ds_read_b128 v[152:155], v210 offset:12288
	ds_read_b128 v[104:107], v210 offset:12800
	ds_read_b128 v[108:111], v210 offset:14336
	ds_read_b128 v[100:103], v210 offset:14848
	s_nop 1
	v_exp_f32_e32 v52, v20
	v_exp_f32_e32 v53, v21
	v_exp_f32_e32 v54, v22
	v_exp_f32_e32 v55, v23
	v_exp_f32_e32 v56, v24
	v_exp_f32_e32 v57, v25
	v_exp_f32_e32 v58, v26
	v_exp_f32_e32 v59, v27
	v_exp_f32_e32 v60, v28
	v_exp_f32_e32 v61, v29
	v_exp_f32_e32 v62, v30
	v_exp_f32_e32 v63, v31
	v_exp_f32_e32 v64, v32
	v_exp_f32_e32 v65, v33
	v_exp_f32_e32 v66, v34
	v_exp_f32_e32 v67, v35
	v_exp_f32_e32 v36, v4
	v_exp_f32_e32 v37, v5
	v_exp_f32_e32 v38, v6
	v_exp_f32_e32 v39, v7
	v_exp_f32_e32 v40, v8
	v_exp_f32_e32 v41, v9
	v_exp_f32_e32 v42, v10
	v_exp_f32_e32 v43, v11
	v_mov_b32_e32 v44, v12
	v_mov_b32_e32 v45, v13
	v_mov_b32_e32 v46, v14
	v_mov_b32_e32 v47, v15
	v_mov_b32_e32 v48, v16
	v_mov_b32_e32 v49, v17
	v_mov_b32_e32 v50, v18
	v_mov_b32_e32 v51, v19
	s_waitcnt vmcnt(4) lgkmcnt(0)
	s_barrier
	v_mov_b32_e32 v4, 0
	v_mov_b32_e32 v5, v2
	v_mov_b32_e32 v6, v2
	v_mov_b32_e32 v7, v2
	v_mov_b32_e32 v8, v2
	v_mov_b32_e32 v9, v2
	v_mov_b32_e32 v10, v2
	v_mov_b32_e32 v11, v2
	v_mov_b32_e32 v12, v2
	v_mov_b32_e32 v13, v2
	v_mov_b32_e32 v14, v2
	v_mov_b32_e32 v15, v2
	v_mov_b32_e32 v16, v2
	v_mov_b32_e32 v17, v2
	v_mov_b32_e32 v18, v2
	v_mov_b32_e32 v19, v2
	v_mov_b32_e32 v20, 0
	v_mov_b32_e32 v21, v2
	v_mov_b32_e32 v22, v2
	v_mov_b32_e32 v23, v2
	v_mov_b32_e32 v24, v2
	v_mov_b32_e32 v25, v2
	v_mov_b32_e32 v26, v2
	v_mov_b32_e32 v27, v2
	v_mov_b32_e32 v28, v2
	v_mov_b32_e32 v29, v2
	v_mov_b32_e32 v30, v2
	v_mov_b32_e32 v31, v2
	v_mov_b32_e32 v32, v2
	v_mov_b32_e32 v33, v2
	v_mov_b32_e32 v34, v2
	v_mov_b32_e32 v35, v2

.LBB0_591:
	s_lshl_b32 s86, s85, 5
	s_add_i32 s44, s86, s43
	s_ashr_i32 s45, s44, 31
	s_add_u32 s0, s44, s21
	s_addc_u32 s1, s45, 0
	s_lshl_b64 s[6:7], s[0:1], 12
	s_add_u32 s6, s12, s6
	s_addc_u32 s7, s13, s7
	v_lshl_add_u64 v[2:3], v[66:67], 4, s[6:7]
	s_mov_b64 s[6:7], 0x1000
	v_lshl_add_u64 v[4:5], v[2:3], 0, s[6:7]
	v_add_co_u32_e32 v6, vcc, s61, v2
	s_mov_b64 s[6:7], 0x2000
	s_nop 0
	v_addc_co_u32_e32 v7, vcc, 0, v3, vcc
	v_lshl_add_u64 v[8:9], v[2:3], 0, s[6:7]
	s_mov_b64 s[6:7], 0x3000
	global_load_dwordx4 v[80:83], v[2:3], off nt
	global_load_dwordx4 v[84:87], v[2:3], off offset:1024 nt
	global_load_dwordx4 v[88:91], v[2:3], off offset:2048 nt
	global_load_dwordx4 v[92:95], v[2:3], off offset:3072 nt
	global_load_dwordx4 v[96:99], v[4:5], off offset:1024 nt
	global_load_dwordx4 v[172:175], v[4:5], off offset:2048 nt
	global_load_dwordx4 v[100:103], v[6:7], off offset:-4096 nt
	global_load_dwordx4 v[62:65], v[6:7], off nt
	global_load_dwordx4 v[176:179], v[4:5], off offset:3072 nt
	global_load_dwordx4 v[58:61], v[8:9], off offset:1024 nt
	global_load_dwordx4 v[54:57], v[8:9], off offset:2048 nt
	global_load_dwordx4 v[50:53], v[8:9], off offset:3072 nt
	v_lshl_add_u64 v[4:5], v[2:3], 0, s[6:7]
	s_movk_i32 s6, 0x3000
	v_add_co_u32_e32 v2, vcc, s6, v2
	s_nop 1
	v_addc_co_u32_e32 v3, vcc, 0, v3, vcc
	global_load_dwordx4 v[10:13], v[4:5], off offset:1024 nt
	global_load_dwordx4 v[6:9], v[4:5], off offset:2048 nt
	global_load_dwordx4 v[14:17], v[2:3], off nt
	s_nop 0
	global_load_dwordx4 v[2:5], v[4:5], off offset:3072 nt
	s_waitcnt vmcnt(15)
	v_and_b32_e32 v149, 0xffff0000, v80
	s_waitcnt vmcnt(9)
	v_and_b32_e32 v115, 0xffff0000, v100
	v_lshlrev_b32_e32 v148, 16, v80
	v_lshlrev_b32_e32 v108, 16, v103
	v_and_b32_e32 v109, 0xffff0000, v103
	v_lshlrev_b32_e32 v110, 16, v102
	v_and_b32_e32 v111, 0xffff0000, v102
	v_lshlrev_b32_e32 v114, 16, v100
	v_mov_b32_e32 v102, v115
	v_mov_b32_e32 v103, v149
	v_lshlrev_b32_e32 v146, 16, v81
	v_lshlrev_b32_e32 v112, 16, v101
	v_and_b32_e32 v113, 0xffff0000, v101
	v_mov_b32_e32 v100, v114
	v_mov_b32_e32 v101, v148
	v_pk_mul_f32 v[102:103], v[102:103], v[102:103]
	v_and_b32_e32 v147, 0xffff0000, v81
	v_lshlrev_b32_e32 v120, 16, v93
	v_and_b32_e32 v121, 0xffff0000, v93
	v_lshlrev_b32_e32 v122, 16, v92
	v_and_b32_e32 v123, 0xffff0000, v92
	v_mov_b32_e32 v92, v112
	v_mov_b32_e32 v93, v146
	v_pk_fma_f32 v[100:101], v[100:101], v[100:101], v[102:103]
	v_lshlrev_b32_e32 v142, 16, v82
	v_lshlrev_b32_e32 v116, 16, v95
	v_and_b32_e32 v117, 0xffff0000, v95
	v_lshlrev_b32_e32 v118, 16, v94
	v_and_b32_e32 v119, 0xffff0000, v94
	v_mov_b32_e32 v94, v113
	v_mov_b32_e32 v95, v147
	v_pk_fma_f32 v[92:93], v[92:93], v[92:93], v[100:101]
	v_and_b32_e32 v143, 0xffff0000, v82
	v_lshlrev_b32_e32 v132, 16, v87
	v_and_b32_e32 v133, 0xffff0000, v87
	v_lshlrev_b32_e32 v134, 16, v86
	v_and_b32_e32 v135, 0xffff0000, v86
	v_mov_b32_e32 v86, v110
	v_mov_b32_e32 v87, v142
	v_pk_fma_f32 v[92:93], v[94:95], v[94:95], v[92:93]
	v_lshlrev_b32_e32 v140, 16, v83
	v_lshlrev_b32_e32 v124, 16, v91
	v_and_b32_e32 v125, 0xffff0000, v91
	v_lshlrev_b32_e32 v126, 16, v90
	v_and_b32_e32 v127, 0xffff0000, v90
	v_mov_b32_e32 v90, v111
	v_mov_b32_e32 v91, v143
	v_pk_fma_f32 v[86:87], v[86:87], v[86:87], v[92:93]
	v_and_b32_e32 v141, 0xffff0000, v83
	v_lshlrev_b32_e32 v136, 16, v85
	v_and_b32_e32 v137, 0xffff0000, v85
	v_lshlrev_b32_e32 v138, 16, v84
	v_and_b32_e32 v139, 0xffff0000, v84
	v_mov_b32_e32 v84, v108
	v_mov_b32_e32 v85, v140
	v_pk_fma_f32 v[86:87], v[90:91], v[90:91], v[86:87]
	v_mov_b32_e32 v80, v109
	v_mov_b32_e32 v81, v141
	v_pk_fma_f32 v[84:85], v[84:85], v[84:85], v[86:87]
	v_lshlrev_b32_e32 v106, 16, v96
	v_and_b32_e32 v107, 0xffff0000, v96
	v_pk_fma_f32 v[80:81], v[80:81], v[80:81], v[84:85]
	v_mov_b32_e32 v180, v106
	v_mov_b32_e32 v181, v138
	v_lshlrev_b32_e32 v104, 16, v97
	v_mov_b32_e32 v182, v107
	v_mov_b32_e32 v183, v139
	v_pk_fma_f32 v[80:81], v[180:181], v[180:181], v[80:81]
	v_lshlrev_b32_e32 v100, 16, v99
	v_and_b32_e32 v101, 0xffff0000, v99
	v_lshlrev_b32_e32 v102, 16, v98
	v_and_b32_e32 v103, 0xffff0000, v98
	v_and_b32_e32 v105, 0xffff0000, v97
	v_lshlrev_b32_e32 v96, 16, v173
	v_and_b32_e32 v97, 0xffff0000, v173
	v_lshlrev_b32_e32 v98, 16, v172
	v_and_b32_e32 v99, 0xffff0000, v172
	v_mov_b32_e32 v172, v104
	v_mov_b32_e32 v173, v136
	v_pk_fma_f32 v[80:81], v[182:183], v[182:183], v[80:81]
	v_lshlrev_b32_e32 v92, 16, v175
	v_and_b32_e32 v93, 0xffff0000, v175
	v_lshlrev_b32_e32 v94, 16, v174
	v_and_b32_e32 v95, 0xffff0000, v174
	v_mov_b32_e32 v174, v105
	v_mov_b32_e32 v175, v137
	v_pk_fma_f32 v[80:81], v[172:173], v[172:173], v[80:81]
	v_mov_b32_e32 v90, v102
	v_mov_b32_e32 v91, v134
	v_pk_fma_f32 v[80:81], v[174:175], v[174:175], v[80:81]
	v_mov_b32_e32 v150, v103
	v_mov_b32_e32 v151, v135
	v_pk_fma_f32 v[80:81], v[90:91], v[90:91], v[80:81]
	v_mov_b32_e32 v84, v100
	v_mov_b32_e32 v85, v132
	v_pk_fma_f32 v[80:81], v[150:151], v[150:151], v[80:81]
	v_lshlrev_b32_e32 v130, 16, v88
	v_mov_b32_e32 v86, v101
	v_mov_b32_e32 v87, v133
	v_pk_fma_f32 v[80:81], v[84:85], v[84:85], v[80:81]
	v_and_b32_e32 v131, 0xffff0000, v88
	v_pk_fma_f32 v[80:81], v[86:87], v[86:87], v[80:81]
	v_mov_b32_e32 v84, v98
	v_mov_b32_e32 v85, v130
	v_lshlrev_b32_e32 v128, 16, v89
	v_mov_b32_e32 v86, v99
	v_mov_b32_e32 v87, v131
	v_pk_fma_f32 v[80:81], v[84:85], v[84:85], v[80:81]
	v_and_b32_e32 v129, 0xffff0000, v89
	v_mov_b32_e32 v144, v96
	v_mov_b32_e32 v145, v128
	v_pk_fma_f32 v[150:151], v[86:87], v[86:87], v[80:81]
	v_mov_b32_e32 v184, v97
	v_mov_b32_e32 v185, v129
	v_pk_fma_f32 v[144:145], v[144:145], v[144:145], v[150:151]
	v_mov_b32_e32 v180, v94
	v_mov_b32_e32 v181, v126
	v_pk_fma_f32 v[144:145], v[184:185], v[184:185], v[144:145]
	v_mov_b32_e32 v182, v95
	v_mov_b32_e32 v183, v127
	v_pk_fma_f32 v[144:145], v[180:181], v[180:181], v[144:145]
	s_waitcnt vmcnt(7)
	v_lshlrev_b32_e32 v86, 16, v177
	v_and_b32_e32 v87, 0xffff0000, v177
	v_lshlrev_b32_e32 v90, 16, v176
	v_and_b32_e32 v91, 0xffff0000, v176
	v_mov_b32_e32 v176, v92
	v_mov_b32_e32 v177, v124
	v_pk_fma_f32 v[144:145], v[182:183], v[182:183], v[144:145]
	v_lshlrev_b32_e32 v80, 16, v179
	v_and_b32_e32 v81, 0xffff0000, v179
	v_lshlrev_b32_e32 v84, 16, v178
	v_and_b32_e32 v85, 0xffff0000, v178
	v_mov_b32_e32 v178, v93
	v_mov_b32_e32 v179, v125
	v_pk_fma_f32 v[144:145], v[176:177], v[176:177], v[144:145]
	v_mov_b32_e32 v180, v91
	v_pk_fma_f32 v[144:145], v[178:179], v[178:179], v[144:145]
	v_mov_b32_e32 v178, v90
	v_mov_b32_e32 v179, v122
	v_mov_b32_e32 v181, v123
	v_pk_fma_f32 v[144:145], v[178:179], v[178:179], v[144:145]
	v_mov_b32_e32 v150, v86
	v_mov_b32_e32 v151, v120
	v_pk_fma_f32 v[144:145], v[180:181], v[180:181], v[144:145]
	v_pk_mul_f32 v[88:89], v[118:119], v[118:119]
	v_pk_mul_f32 v[174:175], v[84:85], v[84:85]
	v_mov_b32_e32 v176, v87
	v_mov_b32_e32 v177, v121
	v_pk_fma_f32 v[144:145], v[150:151], v[150:151], v[144:145]
	v_mov_b32_e32 v150, v174
	v_pk_fma_f32 v[144:145], v[176:177], v[176:177], v[144:145]
	v_mov_b32_e32 v151, v88
	v_pk_mul_f32 v[82:83], v[116:117], v[116:117]
	v_pk_mul_f32 v[172:173], v[80:81], v[80:81]
	v_pk_add_f32 v[144:145], v[144:145], v[150:151]
	v_mov_b32_e32 v88, v175
	v_pk_add_f32 v[88:89], v[144:145], v[88:89]
	v_mov_b32_e32 v144, v172
	v_mov_b32_e32 v145, v82
	v_pk_add_f32 v[88:89], v[88:89], v[144:145]
	v_mov_b32_e32 v82, v173
	v_pk_add_f32 v[82:83], v[88:89], v[82:83]
	ds_bpermute_b32 v89, v1, v83
	ds_bpermute_b32 v88, v1, v82
	v_mov_b32_e32 v173, 0
	s_lshl_b64 s[0:1], s[0:1], 11
	v_lshl_add_u64 v[144:145], v[76:77], 0, s[0:1]
	s_add_u32 s0, s55, s44
	s_waitcnt lgkmcnt(0)
	v_pk_add_f32 v[82:83], v[82:83], v[88:89]
	ds_bpermute_b32 v89, v152, v83
	ds_bpermute_b32 v88, v152, v82
	s_addc_u32 s1, s45, 0
	s_lshl_b64 s[0:1], s[0:1], 11
	v_mov_b32_e32 v172, 0
	s_waitcnt lgkmcnt(0)
	v_pk_add_f32 v[82:83], v[82:83], v[88:89]
	ds_bpermute_b32 v89, v153, v83
	ds_bpermute_b32 v88, v153, v82
	s_waitcnt lgkmcnt(0)
	v_pk_add_f32 v[82:83], v[82:83], v[88:89]
	ds_bpermute_b32 v89, v154, v83
	ds_bpermute_b32 v88, v154, v82
	s_waitcnt lgkmcnt(0)
	v_pk_add_f32 v[82:83], v[82:83], v[88:89]
	ds_bpermute_b32 v89, v155, v83
	ds_bpermute_b32 v88, v155, v82
	s_waitcnt lgkmcnt(0)
	v_pk_add_f32 v[82:83], v[82:83], v[88:89]
	ds_bpermute_b32 v89, v156, v83
	ds_bpermute_b32 v88, v156, v82
	s_waitcnt lgkmcnt(0)
	v_pk_add_f32 v[88:89], v[82:83], v[88:89]
	v_mov_b64_e32 v[82:83], s[20:21]
	v_pk_fma_f32 v[150:151], v[88:89], s[18:19], v[82:83] op_sel_hi:[1,0,0]
	v_lshl_add_u64 v[88:89], v[76:77], 0, s[0:1]
	v_mul_f32_e32 v0, 0x4b800000, v151
	v_cmp_gt_f32_e32 vcc, s62, v151
	s_add_u32 s0, s57, s44
	s_addc_u32 s1, s45, 0
	v_cndmask_b32_e32 v0, v151, v0, vcc
	v_rsq_f32_e32 v0, v0
	s_lshl_b64 s[0:1], s[0:1], 11
	v_mul_f32_e32 v72, 0x45800000, v0
	v_cndmask_b32_e32 v0, v0, v72, vcc
	v_pk_mul_f32 v[148:149], v[0:1], v[148:149] op_sel_hi:[0,1]
	v_pk_mul_f32 v[146:147], v[0:1], v[146:147] op_sel_hi:[0,1]
	v_pk_mul_f32 v[142:143], v[0:1], v[142:143] op_sel_hi:[0,1]
	v_pk_mul_f32 v[140:141], v[0:1], v[140:141] op_sel_hi:[0,1]
	v_pk_mul_f32 v[148:149], v[42:43], v[148:149]
	v_pk_mul_f32 v[146:147], v[44:45], v[146:147]
	v_pk_mul_f32 v[142:143], v[46:47], v[142:143]
	v_pk_mul_f32 v[174:175], v[48:49], v[140:141]
	v_cvt_pk_fp8_f32 v173, v142, v143
	v_cvt_pk_bf16_f32 v140, v148, v149
	v_cvt_pk_bf16_f32 v141, v146, v147
	v_cvt_pk_bf16_f32 v142, v142, v143
	v_cvt_pk_bf16_f32 v143, v174, v175
	v_add_u32_e32 v72, s52, v161
	v_pk_mul_f32 v[138:139], v[0:1], v[138:139] op_sel_hi:[0,1]
	v_pk_mul_f32 v[136:137], v[0:1], v[136:137] op_sel_hi:[0,1]
	v_pk_mul_f32 v[134:135], v[0:1], v[134:135] op_sel_hi:[0,1]
	v_pk_mul_f32 v[132:133], v[0:1], v[132:133] op_sel_hi:[0,1]
	ds_write_b128 v72, v[140:143]
	v_pk_mul_f32 v[138:139], v[34:35], v[138:139]
	v_pk_mul_f32 v[136:137], v[36:37], v[136:137]
	v_pk_mul_f32 v[134:135], v[38:39], v[134:135]
	v_mov_b32_e32 v141, 0
	v_pk_mul_f32 v[142:143], v[40:41], v[132:133]
	v_pk_mul_f32 v[130:131], v[0:1], v[130:131] op_sel_hi:[0,1]
	v_pk_mul_f32 v[128:129], v[0:1], v[128:129] op_sel_hi:[0,1]
	v_pk_mul_f32 v[126:127], v[0:1], v[126:127] op_sel_hi:[0,1]
	v_pk_mul_f32 v[124:125], v[0:1], v[124:125] op_sel_hi:[0,1]
	v_pk_mul_f32 v[122:123], v[0:1], v[122:123] op_sel_hi:[0,1]
	v_pk_mul_f32 v[120:121], v[0:1], v[120:121] op_sel_hi:[0,1]
	v_pk_mul_f32 v[118:119], v[0:1], v[118:119] op_sel_hi:[0,1]
	v_pk_mul_f32 v[116:117], v[0:1], v[116:117] op_sel_hi:[0,1]
	v_mul_f32_e32 v0, 0x4b800000, v150
	v_cmp_gt_f32_e32 vcc, s62, v150
	v_cvt_pk_fp8_f32 v141, v134, v135
	v_cvt_pk_bf16_f32 v132, v138, v139
	v_cvt_pk_bf16_f32 v133, v136, v137
	v_cvt_pk_bf16_f32 v134, v134, v135
	v_cvt_pk_bf16_f32 v135, v142, v143
	v_add_u32_e32 v72, s52, v162
	v_cndmask_b32_e32 v0, v150, v0, vcc
	ds_write_b128 v72, v[132:135]
	v_pk_mul_f32 v[130:131], v[26:27], v[130:131]
	v_pk_mul_f32 v[128:129], v[28:29], v[128:129]
	v_pk_mul_f32 v[126:127], v[30:31], v[126:127]
	v_mov_b32_e32 v133, 0
	v_pk_mul_f32 v[134:135], v[32:33], v[124:125]
	v_rsq_f32_e32 v0, v0
	v_cvt_pk_fp8_f32 v133, v126, v127
	v_cvt_pk_bf16_f32 v124, v130, v131
	v_cvt_pk_bf16_f32 v125, v128, v129
	v_cvt_pk_bf16_f32 v126, v126, v127
	v_cvt_pk_bf16_f32 v127, v134, v135
	v_add_u32_e32 v72, s52, v163
	ds_write_b128 v72, v[124:127]
	v_pk_mul_f32 v[122:123], v[18:19], v[122:123]
	v_pk_mul_f32 v[120:121], v[20:21], v[120:121]
	v_pk_mul_f32 v[118:119], v[22:23], v[118:119]
	v_pk_mul_f32 v[124:125], v[24:25], v[116:117]
	v_mov_b32_e32 v127, 0
	v_cvt_pk_bf16_f32 v116, v122, v123
	v_cvt_pk_bf16_f32 v117, v120, v121
	v_cvt_pk_fp8_f32 v127, v118, v119
	v_cvt_pk_bf16_f32 v118, v118, v119
	v_cvt_pk_bf16_f32 v119, v124, v125
	v_add_u32_e32 v72, s52, v164
	ds_write_b128 v72, v[116:119]
	v_mul_f32_e32 v72, 0x45800000, v0
	v_cndmask_b32_e32 v72, v0, v72, vcc
	v_pk_mul_f32 v[114:115], v[72:73], v[114:115] op_sel_hi:[0,1]
	v_pk_mul_f32 v[112:113], v[72:73], v[112:113] op_sel_hi:[0,1]
	v_pk_mul_f32 v[110:111], v[72:73], v[110:111] op_sel_hi:[0,1]
	v_pk_mul_f32 v[108:109], v[72:73], v[108:109] op_sel_hi:[0,1]
	v_pk_mul_f32 v[114:115], v[42:43], v[114:115]
	v_pk_mul_f32 v[112:113], v[44:45], v[112:113]
	v_pk_mul_f32 v[110:111], v[46:47], v[110:111]
	v_mov_b32_e32 v117, 0
	v_pk_mul_f32 v[118:119], v[48:49], v[108:109]
	v_cvt_pk_fp8_f32 v117, v110, v111
	v_cvt_pk_bf16_f32 v108, v114, v115
	v_cvt_pk_bf16_f32 v109, v112, v113
	v_cvt_pk_bf16_f32 v110, v110, v111
	v_cvt_pk_bf16_f32 v111, v118, v119
	v_add_u32_e32 v0, s56, v161
	v_pk_mul_f32 v[106:107], v[72:73], v[106:107] op_sel_hi:[0,1]
	v_pk_mul_f32 v[104:105], v[72:73], v[104:105] op_sel_hi:[0,1]
	v_pk_mul_f32 v[102:103], v[72:73], v[102:103] op_sel_hi:[0,1]
	v_pk_mul_f32 v[100:101], v[72:73], v[100:101] op_sel_hi:[0,1]
	ds_write_b128 v0, v[108:111]
	v_pk_mul_f32 v[106:107], v[34:35], v[106:107]
	v_pk_mul_f32 v[104:105], v[36:37], v[104:105]
	v_pk_mul_f32 v[102:103], v[38:39], v[102:103]
	v_mov_b32_e32 v109, 0
	v_pk_mul_f32 v[110:111], v[40:41], v[100:101]
	v_cvt_pk_fp8_f32 v109, v102, v103
	v_cvt_pk_bf16_f32 v100, v106, v107
	v_cvt_pk_bf16_f32 v101, v104, v105
	v_cvt_pk_bf16_f32 v102, v102, v103
	v_cvt_pk_bf16_f32 v103, v110, v111
	v_add_u32_e32 v0, s56, v162
	v_pk_mul_f32 v[98:99], v[72:73], v[98:99] op_sel_hi:[0,1]
	v_pk_mul_f32 v[94:95], v[72:73], v[94:95] op_sel_hi:[0,1]
	ds_write_b128 v0, v[100:103]
	v_pk_mul_f32 v[98:99], v[26:27], v[98:99]
	v_pk_mul_f32 v[94:95], v[30:31], v[94:95]
	v_mov_b32_e32 v100, 0
	v_mov_b32_e32 v101, 0
	v_mov_b32_e32 v116, 0
	v_cvt_pk_fp8_f32 v100, v98, v99
	v_cvt_pk_fp8_f32 v101, v94, v95
	v_cvt_pk_fp8_f32 v116, v114, v115
	v_mov_b32_e32 v108, 0
	v_pk_mul_f32 v[96:97], v[72:73], v[96:97] op_sel_hi:[0,1]
	v_pk_mul_f32 v[92:93], v[72:73], v[92:93] op_sel_hi:[0,1]
	v_mov_b32_e32 v126, 0
	v_cvt_pk_fp8_f32 v108, v106, v107
	v_pk_mul_f32 v[96:97], v[28:29], v[96:97]
	v_pk_mul_f32 v[102:103], v[32:33], v[92:93]
	v_cvt_pk_fp8_f32 v126, v122, v123
	v_cvt_pk_fp8_f32 v100, v96, v97 op_sel:[0,0,1]
	v_cvt_pk_fp8_f32 v101, v102, v103 op_sel:[0,0,1]
	v_mov_b32_e32 v132, 0
	v_cvt_pk_fp8_f32 v116, v112, v113 op_sel:[0,0,1]
	v_cvt_pk_fp8_f32 v117, v118, v119 op_sel:[0,0,1]
	v_pk_mul_f32 v[90:91], v[72:73], v[90:91] op_sel_hi:[0,1]
	v_mov_b32_e32 v140, 0
	v_cvt_pk_fp8_f32 v132, v130, v131
	v_cvt_pk_fp8_f32 v127, v124, v125 op_sel:[0,0,1]
	v_pk_mul_f32 v[122:123], v[18:19], v[90:91]
	v_and_b32_e32 v125, 0xffff0000, v62
	s_waitcnt vmcnt(1)
	v_and_b32_e32 v91, 0xffff0000, v14
	v_cvt_pk_fp8_f32 v140, v138, v139
	v_cvt_pk_fp8_f32 v108, v104, v105 op_sel:[0,0,1]
	v_cvt_pk_fp8_f32 v109, v110, v111 op_sel:[0,0,1]
	v_lshlrev_b32_e32 v124, 16, v62
	v_lshlrev_b32_e32 v112, 16, v59
	v_and_b32_e32 v113, 0xffff0000, v59
	v_lshlrev_b32_e32 v114, 16, v58
	v_and_b32_e32 v115, 0xffff0000, v58
	v_lshlrev_b32_e32 v90, 16, v14
	v_mov_b32_e32 v58, v91
	v_mov_b32_e32 v59, v125
	v_cvt_pk_fp8_f32 v126, v120, v121 op_sel:[0,0,1]
	v_cvt_pk_bf16_f32 v92, v98, v99
	v_cvt_pk_bf16_f32 v93, v96, v97
	v_cvt_pk_bf16_f32 v94, v94, v95
	v_cvt_pk_bf16_f32 v95, v102, v103
	global_store_dwordx2 v[88:89], v[100:101], off offset:1024
	v_add_u32_e32 v0, s56, v163
	v_lshlrev_b32_e32 v118, 16, v64
	v_and_b32_e32 v119, 0xffff0000, v64
	v_lshlrev_b32_e32 v120, 16, v63
	v_lshlrev_b32_e32 v100, 16, v57
	v_and_b32_e32 v101, 0xffff0000, v57
	v_lshlrev_b32_e32 v102, 16, v56
	v_and_b32_e32 v103, 0xffff0000, v56
	v_lshlrev_b32_e32 v64, 16, v15
	v_mov_b32_e32 v56, v90
	v_mov_b32_e32 v57, v124
	v_pk_mul_f32 v[58:59], v[58:59], v[58:59]
	global_store_dwordx2 v[88:89], v[116:117], off
	ds_write_b128 v0, v[92:95]
	v_lshlrev_b32_e32 v116, 16, v65
	v_and_b32_e32 v117, 0xffff0000, v65
	v_and_b32_e32 v121, 0xffff0000, v63
	v_lshlrev_b32_e32 v92, 16, v53
	v_and_b32_e32 v93, 0xffff0000, v53
	v_lshlrev_b32_e32 v94, 16, v52
	v_and_b32_e32 v95, 0xffff0000, v52
	v_and_b32_e32 v65, 0xffff0000, v15
	v_mov_b32_e32 v52, v64
	v_mov_b32_e32 v53, v120
	v_pk_fma_f32 v[56:57], v[56:57], v[56:57], v[58:59]
	v_cvt_pk_fp8_f32 v132, v128, v129 op_sel:[0,0,1]
	v_cvt_pk_fp8_f32 v133, v134, v135 op_sel:[0,0,1]
	v_lshlrev_b32_e32 v104, 16, v55
	v_and_b32_e32 v105, 0xffff0000, v55
	v_lshlrev_b32_e32 v106, 16, v54
	v_and_b32_e32 v107, 0xffff0000, v54
	v_lshlrev_b32_e32 v62, 16, v16
	v_mov_b32_e32 v54, v65
	v_mov_b32_e32 v55, v121
	v_pk_fma_f32 v[52:53], v[52:53], v[52:53], v[56:57]
	v_cvt_pk_fp8_f32 v140, v136, v137 op_sel:[0,0,1]
	v_cvt_pk_fp8_f32 v141, v142, v143 op_sel:[0,0,1]
	global_store_dwordx2 v[88:89], v[108:109], off offset:512
	v_lshlrev_b32_e32 v108, 16, v61
	v_and_b32_e32 v109, 0xffff0000, v61
	v_lshlrev_b32_e32 v110, 16, v60
	v_and_b32_e32 v111, 0xffff0000, v60
	v_lshlrev_b32_e32 v60, 16, v17
	v_and_b32_e32 v61, 0xffff0000, v17
	v_and_b32_e32 v63, 0xffff0000, v16
	v_mov_b32_e32 v16, v62
	v_mov_b32_e32 v17, v118
	v_pk_fma_f32 v[52:53], v[54:55], v[54:55], v[52:53]
	v_lshlrev_b32_e32 v96, 16, v51
	v_and_b32_e32 v97, 0xffff0000, v51
	v_lshlrev_b32_e32 v98, 16, v50
	v_and_b32_e32 v99, 0xffff0000, v50
	v_mov_b32_e32 v50, v63
	v_mov_b32_e32 v51, v119
	v_pk_fma_f32 v[16:17], v[16:17], v[16:17], v[52:53]
	v_mov_b32_e32 v14, v60
	v_mov_b32_e32 v15, v116
	v_pk_fma_f32 v[16:17], v[50:51], v[50:51], v[16:17]
	global_store_dwordx2 v[144:145], v[132:133], off offset:1024
	v_mov_b32_e32 v130, v61
	v_mov_b32_e32 v131, v117
	v_pk_fma_f32 v[132:133], v[14:15], v[14:15], v[16:17]
	v_lshlrev_b32_e32 v58, 16, v10
	global_store_dwordx2 v[144:145], v[140:141], off offset:512
	v_and_b32_e32 v59, 0xffff0000, v10
	v_lshlrev_b32_e32 v16, 16, v7
	v_and_b32_e32 v17, 0xffff0000, v7
	v_lshlrev_b32_e32 v50, 16, v6
	v_and_b32_e32 v51, 0xffff0000, v6
	v_pk_fma_f32 v[6:7], v[130:131], v[130:131], v[132:133]
	v_mov_b32_e32 v140, v58
	v_mov_b32_e32 v141, v114
	v_lshlrev_b32_e32 v56, 16, v11
	v_mov_b32_e32 v142, v59
	v_mov_b32_e32 v143, v115
	v_pk_fma_f32 v[6:7], v[140:141], v[140:141], v[6:7]
	v_and_b32_e32 v57, 0xffff0000, v11
	v_mov_b32_e32 v136, v56
	v_mov_b32_e32 v137, v112
	v_pk_fma_f32 v[6:7], v[142:143], v[142:143], v[6:7]
	v_cvt_pk_fp8_f32 v172, v148, v149
	v_lshlrev_b32_e32 v54, 16, v12
	v_mov_b32_e32 v138, v57
	v_mov_b32_e32 v139, v113
	v_pk_fma_f32 v[6:7], v[136:137], v[136:137], v[6:7]
	v_and_b32_e32 v55, 0xffff0000, v12
	v_mov_b32_e32 v130, v54
	v_mov_b32_e32 v131, v110
	v_pk_fma_f32 v[6:7], v[138:139], v[138:139], v[6:7]
	v_lshlrev_b32_e32 v52, 16, v13
	v_mov_b32_e32 v132, v55
	v_mov_b32_e32 v133, v111
	v_pk_fma_f32 v[6:7], v[130:131], v[130:131], v[6:7]
	v_and_b32_e32 v53, 0xffff0000, v13
	v_lshlrev_b32_e32 v12, 16, v9
	v_and_b32_e32 v13, 0xffff0000, v9
	v_lshlrev_b32_e32 v14, 16, v8
	v_and_b32_e32 v15, 0xffff0000, v8
	v_mov_b32_e32 v8, v52
	v_mov_b32_e32 v9, v108
	v_pk_fma_f32 v[6:7], v[132:133], v[132:133], v[6:7]
	v_cvt_pk_fp8_f32 v172, v146, v147 op_sel:[0,0,1]
	v_cvt_pk_fp8_f32 v173, v174, v175 op_sel:[0,0,1]
	v_mov_b32_e32 v10, v53
	v_mov_b32_e32 v11, v109
	v_pk_fma_f32 v[6:7], v[8:9], v[8:9], v[6:7]
	v_mov_b32_e32 v8, v50
	v_pk_fma_f32 v[6:7], v[10:11], v[10:11], v[6:7]
	v_mov_b32_e32 v9, v106
	v_mov_b32_e32 v10, v51
	v_mov_b32_e32 v11, v107
	v_pk_fma_f32 v[6:7], v[8:9], v[8:9], v[6:7]
	v_mov_b32_e32 v134, v16
	v_mov_b32_e32 v135, v104
	v_pk_fma_f32 v[130:131], v[10:11], v[10:11], v[6:7]
	global_store_dwordx2 v[144:145], v[172:173], off
	global_store_dwordx2 v[144:145], v[126:127], off offset:1536
	v_mov_b32_e32 v144, v17
	v_mov_b32_e32 v145, v105
	v_pk_fma_f32 v[130:131], v[134:135], v[134:135], v[130:131]
	v_mov_b32_e32 v140, v14
	v_mov_b32_e32 v141, v102
	v_pk_fma_f32 v[130:131], v[144:145], v[144:145], v[130:131]
	v_mov_b32_e32 v142, v15
	v_mov_b32_e32 v143, v103
	v_pk_fma_f32 v[130:131], v[140:141], v[140:141], v[130:131]
	s_waitcnt vmcnt(7)
	v_lshlrev_b32_e32 v6, 16, v5
	v_and_b32_e32 v7, 0xffff0000, v5
	v_lshlrev_b32_e32 v8, 16, v4
	v_and_b32_e32 v9, 0xffff0000, v4
	v_lshlrev_b32_e32 v4, 16, v3
	v_and_b32_e32 v5, 0xffff0000, v3
	v_lshlrev_b32_e32 v10, 16, v2
	v_and_b32_e32 v11, 0xffff0000, v2
	v_mov_b32_e32 v2, v12
	v_mov_b32_e32 v3, v100
	v_pk_fma_f32 v[130:131], v[142:143], v[142:143], v[130:131]
	v_mov_b32_e32 v138, v13
	v_mov_b32_e32 v139, v101
	v_pk_fma_f32 v[2:3], v[2:3], v[2:3], v[130:131]
	v_mov_b32_e32 v140, v11
	v_pk_fma_f32 v[2:3], v[138:139], v[138:139], v[2:3]
	v_mov_b32_e32 v138, v10
	v_mov_b32_e32 v139, v98
	v_mov_b32_e32 v141, v99
	v_pk_fma_f32 v[2:3], v[138:139], v[138:139], v[2:3]
	v_mov_b32_e32 v130, v4
	v_mov_b32_e32 v131, v96
	v_pk_fma_f32 v[2:3], v[140:141], v[140:141], v[2:3]
	v_pk_mul_f32 v[128:129], v[94:95], v[94:95]
	v_pk_mul_f32 v[136:137], v[8:9], v[8:9]
	v_mov_b32_e32 v134, v5
	v_mov_b32_e32 v135, v97
	v_pk_fma_f32 v[2:3], v[130:131], v[130:131], v[2:3]
	v_mov_b32_e32 v130, v136
	v_pk_fma_f32 v[2:3], v[134:135], v[134:135], v[2:3]
	v_mov_b32_e32 v131, v128
	v_pk_mul_f32 v[126:127], v[92:93], v[92:93]
	v_pk_mul_f32 v[132:133], v[6:7], v[6:7]
	v_pk_add_f32 v[2:3], v[2:3], v[130:131]
	v_mov_b32_e32 v128, v137
	v_pk_add_f32 v[2:3], v[2:3], v[128:129]
	v_mov_b32_e32 v128, v132
	v_mov_b32_e32 v129, v126
	v_pk_add_f32 v[2:3], v[2:3], v[128:129]
	v_mov_b32_e32 v126, v133
	v_pk_add_f32 v[2:3], v[2:3], v[126:127]
	ds_bpermute_b32 v127, v1, v3
	ds_bpermute_b32 v126, v1, v2
	v_pk_mul_f32 v[86:87], v[72:73], v[86:87] op_sel_hi:[0,1]
	v_pk_mul_f32 v[84:85], v[72:73], v[84:85] op_sel_hi:[0,1]
	v_mov_b32_e32 v130, 0
	v_pk_mul_f32 v[128:129], v[20:21], v[86:87]
	s_waitcnt lgkmcnt(0)
	v_pk_add_f32 v[2:3], v[2:3], v[126:127]
	ds_bpermute_b32 v127, v152, v3
	ds_bpermute_b32 v126, v152, v2
	v_pk_mul_f32 v[86:87], v[22:23], v[84:85]
	v_cvt_pk_bf16_f32 v84, v122, v123
	v_cvt_pk_fp8_f32 v130, v122, v123
	v_mov_b32_e32 v131, 0
	s_waitcnt lgkmcnt(0)
	v_pk_add_f32 v[2:3], v[2:3], v[126:127]
	ds_bpermute_b32 v127, v153, v3
	ds_bpermute_b32 v126, v153, v2
	v_cvt_pk_fp8_f32 v131, v86, v87
	v_pk_mul_f32 v[80:81], v[72:73], v[80:81] op_sel_hi:[0,1]
	v_pk_mul_f32 v[80:81], v[24:25], v[80:81]
	v_cvt_pk_bf16_f32 v86, v86, v87
	s_waitcnt lgkmcnt(0)
	v_pk_add_f32 v[2:3], v[2:3], v[126:127]
	ds_bpermute_b32 v123, v154, v3
	ds_bpermute_b32 v122, v154, v2
	v_cvt_pk_bf16_f32 v87, v80, v81
	v_cvt_pk_fp8_f32 v131, v80, v81 op_sel:[0,0,1]
	v_cvt_pk_bf16_f32 v85, v128, v129
	v_add_u32_e32 v0, s56, v164
	s_waitcnt lgkmcnt(0)
	v_pk_add_f32 v[2:3], v[2:3], v[122:123]
	ds_bpermute_b32 v81, v155, v3
	ds_bpermute_b32 v80, v155, v2
	ds_write_b128 v0, v[84:87]
	v_cvt_pk_fp8_f32 v130, v128, v129 op_sel:[0,0,1]
	s_waitcnt lgkmcnt(1)
	v_pk_add_f32 v[2:3], v[2:3], v[80:81]
	ds_bpermute_b32 v85, v156, v3
	ds_bpermute_b32 v84, v156, v2
	global_store_dwordx2 v[88:89], v[130:131], off offset:1536
	v_lshl_add_u64 v[80:81], v[76:77], 0, s[0:1]
	s_add_u32 s0, s59, s44
	s_addc_u32 s1, s45, 0
	s_waitcnt lgkmcnt(0)
	v_pk_add_f32 v[2:3], v[2:3], v[84:85]
	s_lshl_b64 s[0:1], s[0:1], 11
	v_pk_fma_f32 v[82:83], v[2:3], s[18:19], v[82:83] op_sel_hi:[1,0,0]
	v_lshl_add_u64 v[2:3], v[76:77], 0, s[0:1]
	v_mul_f32_e32 v0, 0x4b800000, v83
	v_cmp_gt_f32_e32 vcc, s62, v83
	s_mov_b32 s0, 0
	s_nop 0
	v_cndmask_b32_e32 v0, v83, v0, vcc
	v_rsq_f32_e32 v0, v0
	v_mov_b32_e32 v83, 0
	v_mul_f32_e32 v72, 0x45800000, v0
	v_cndmask_b32_e32 v0, v0, v72, vcc
	v_pk_mul_f32 v[84:85], v[0:1], v[124:125] op_sel_hi:[0,1]
	v_pk_mul_f32 v[84:85], v[42:43], v[84:85]
	v_pk_mul_f32 v[88:89], v[0:1], v[118:119] op_sel_hi:[0,1]
	v_mov_b32_e32 v118, 0
	v_cvt_pk_fp8_f32 v118, v84, v85
	v_pk_mul_f32 v[86:87], v[0:1], v[120:121] op_sel_hi:[0,1]
	v_pk_mul_f32 v[116:117], v[0:1], v[116:117] op_sel_hi:[0,1]
	v_pk_mul_f32 v[86:87], v[44:45], v[86:87]
	v_pk_mul_f32 v[88:89], v[46:47], v[88:89]
	v_pk_mul_f32 v[116:117], v[48:49], v[116:117]
	v_cvt_pk_bf16_f32 v84, v84, v85
	v_cvt_pk_fp8_f32 v118, v86, v87 op_sel:[0,0,1]
	v_cvt_pk_bf16_f32 v85, v86, v87
	v_cvt_pk_bf16_f32 v86, v88, v89
	v_cvt_pk_bf16_f32 v87, v116, v117
	v_add_u32_e32 v72, s58, v161
	v_mov_b32_e32 v119, 0
	ds_write_b128 v72, v[84:87]
	v_pk_mul_f32 v[84:85], v[0:1], v[114:115] op_sel_hi:[0,1]
	v_cvt_pk_fp8_f32 v119, v88, v89
	v_pk_mul_f32 v[84:85], v[34:35], v[84:85]
	v_pk_mul_f32 v[88:89], v[0:1], v[110:111] op_sel_hi:[0,1]
	v_mov_b32_e32 v110, 0
	v_cvt_pk_fp8_f32 v110, v84, v85
	v_pk_mul_f32 v[86:87], v[0:1], v[112:113] op_sel_hi:[0,1]
	v_pk_mul_f32 v[108:109], v[0:1], v[108:109] op_sel_hi:[0,1]
	v_pk_mul_f32 v[86:87], v[36:37], v[86:87]
	v_pk_mul_f32 v[88:89], v[38:39], v[88:89]
	v_pk_mul_f32 v[108:109], v[40:41], v[108:109]
	v_cvt_pk_bf16_f32 v84, v84, v85
	v_cvt_pk_fp8_f32 v110, v86, v87 op_sel:[0,0,1]
	v_cvt_pk_bf16_f32 v85, v86, v87
	v_cvt_pk_bf16_f32 v86, v88, v89
	v_cvt_pk_bf16_f32 v87, v108, v109
	v_add_u32_e32 v72, s58, v162
	v_mov_b32_e32 v111, 0
	ds_write_b128 v72, v[84:87]
	v_pk_mul_f32 v[84:85], v[0:1], v[106:107] op_sel_hi:[0,1]
	v_cvt_pk_fp8_f32 v111, v88, v89
	v_pk_mul_f32 v[84:85], v[26:27], v[84:85]
	v_pk_mul_f32 v[88:89], v[0:1], v[102:103] op_sel_hi:[0,1]
	v_mov_b32_e32 v102, 0
	v_cvt_pk_fp8_f32 v102, v84, v85
	v_pk_mul_f32 v[86:87], v[0:1], v[104:105] op_sel_hi:[0,1]
	v_pk_mul_f32 v[100:101], v[0:1], v[100:101] op_sel_hi:[0,1]
	v_pk_mul_f32 v[86:87], v[28:29], v[86:87]
	v_pk_mul_f32 v[88:89], v[30:31], v[88:89]
	v_pk_mul_f32 v[100:101], v[32:33], v[100:101]
	v_cvt_pk_bf16_f32 v84, v84, v85
	v_cvt_pk_fp8_f32 v102, v86, v87 op_sel:[0,0,1]
	v_cvt_pk_bf16_f32 v85, v86, v87
	v_cvt_pk_bf16_f32 v86, v88, v89
	v_cvt_pk_bf16_f32 v87, v100, v101
	v_add_u32_e32 v72, s58, v163
	ds_write_b128 v72, v[84:87]
	v_pk_mul_f32 v[84:85], v[0:1], v[98:99] op_sel_hi:[0,1]
	v_mov_b32_e32 v103, 0
	v_pk_mul_f32 v[86:87], v[18:19], v[84:85]
	v_pk_mul_f32 v[84:85], v[0:1], v[96:97] op_sel_hi:[0,1]
	v_cvt_pk_fp8_f32 v103, v88, v89
	v_pk_mul_f32 v[88:89], v[20:21], v[84:85]
	v_pk_mul_f32 v[84:85], v[0:1], v[94:95] op_sel_hi:[0,1]
	v_pk_mul_f32 v[94:95], v[22:23], v[84:85]
	v_mov_b32_e32 v96, 0
	v_mov_b32_e32 v97, 0
	v_pk_mul_f32 v[84:85], v[0:1], v[92:93] op_sel_hi:[0,1]
	v_cvt_pk_fp8_f32 v96, v86, v87
	v_cvt_pk_fp8_f32 v97, v94, v95
	v_mul_f32_e32 v0, 0x4b800000, v82
	v_cmp_gt_f32_e32 vcc, s62, v82
	v_pk_mul_f32 v[92:93], v[24:25], v[84:85]
	v_cvt_pk_fp8_f32 v119, v116, v117 op_sel:[0,0,1]
	v_cndmask_b32_e32 v0, v82, v0, vcc
	v_rsq_f32_e32 v0, v0
	v_cvt_pk_fp8_f32 v111, v108, v109 op_sel:[0,0,1]
	v_cvt_pk_fp8_f32 v103, v100, v101 op_sel:[0,0,1]
	v_cvt_pk_fp8_f32 v96, v88, v89 op_sel:[0,0,1]
	v_cvt_pk_fp8_f32 v97, v92, v93 op_sel:[0,0,1]
	v_cvt_pk_bf16_f32 v84, v86, v87
	v_cvt_pk_bf16_f32 v85, v88, v89
	v_cvt_pk_bf16_f32 v86, v94, v95
	v_cvt_pk_bf16_f32 v87, v92, v93
	v_add_u32_e32 v72, s58, v164
	ds_write_b128 v72, v[84:87]
	v_mul_f32_e32 v72, 0x45800000, v0
	v_cndmask_b32_e32 v0, v0, v72, vcc
	global_store_dwordx2 v[80:81], v[118:119], off
	global_store_dwordx2 v[80:81], v[110:111], off offset:512
	global_store_dwordx2 v[80:81], v[102:103], off offset:1024
	global_store_dwordx2 v[80:81], v[96:97], off offset:1536
	v_pk_mul_f32 v[80:81], v[0:1], v[90:91] op_sel_hi:[0,1]
	v_pk_mul_f32 v[80:81], v[42:43], v[80:81]
	v_mov_b32_e32 v82, 0
	v_cvt_pk_fp8_f32 v82, v80, v81
	v_pk_mul_f32 v[64:65], v[0:1], v[64:65] op_sel_hi:[0,1]
	v_pk_mul_f32 v[62:63], v[0:1], v[62:63] op_sel_hi:[0,1]
	v_pk_mul_f32 v[60:61], v[0:1], v[60:61] op_sel_hi:[0,1]
	v_pk_mul_f32 v[64:65], v[44:45], v[64:65]
	v_pk_mul_f32 v[62:63], v[46:47], v[62:63]
	v_pk_mul_f32 v[84:85], v[48:49], v[60:61]
	v_cvt_pk_fp8_f32 v83, v62, v63
	v_cvt_pk_bf16_f32 v60, v80, v81
	v_cvt_pk_fp8_f32 v82, v64, v65 op_sel:[0,0,1]
	v_cvt_pk_bf16_f32 v61, v64, v65
	v_cvt_pk_bf16_f32 v62, v62, v63
	v_cvt_pk_bf16_f32 v63, v84, v85
	v_add_u32_e32 v64, s60, v161
	v_pk_mul_f32 v[58:59], v[0:1], v[58:59] op_sel_hi:[0,1]
	ds_write_b128 v64, v[60:63]
	v_pk_mul_f32 v[58:59], v[34:35], v[58:59]
	v_mov_b32_e32 v60, 0
	v_cvt_pk_fp8_f32 v60, v58, v59
	v_pk_mul_f32 v[56:57], v[0:1], v[56:57] op_sel_hi:[0,1]
	v_pk_mul_f32 v[54:55], v[0:1], v[54:55] op_sel_hi:[0,1]
	v_pk_mul_f32 v[52:53], v[0:1], v[52:53] op_sel_hi:[0,1]
	v_pk_mul_f32 v[56:57], v[36:37], v[56:57]
	v_pk_mul_f32 v[54:55], v[38:39], v[54:55]
	v_mov_b32_e32 v61, 0
	v_pk_mul_f32 v[62:63], v[40:41], v[52:53]
	v_cvt_pk_fp8_f32 v61, v54, v55
	v_cvt_pk_bf16_f32 v52, v58, v59
	v_cvt_pk_fp8_f32 v60, v56, v57 op_sel:[0,0,1]
	v_cvt_pk_bf16_f32 v53, v56, v57
	v_cvt_pk_bf16_f32 v54, v54, v55
	v_cvt_pk_bf16_f32 v55, v62, v63
	v_add_u32_e32 v56, s60, v162
	v_pk_mul_f32 v[50:51], v[0:1], v[50:51] op_sel_hi:[0,1]
	ds_write_b128 v56, v[52:55]
	v_pk_mul_f32 v[50:51], v[26:27], v[50:51]
	v_mov_b32_e32 v52, 0
	v_cvt_pk_fp8_f32 v52, v50, v51
	v_pk_mul_f32 v[16:17], v[0:1], v[16:17] op_sel_hi:[0,1]
	v_pk_mul_f32 v[14:15], v[0:1], v[14:15] op_sel_hi:[0,1]
	v_pk_mul_f32 v[12:13], v[0:1], v[12:13] op_sel_hi:[0,1]
	v_pk_mul_f32 v[16:17], v[28:29], v[16:17]
	v_pk_mul_f32 v[14:15], v[30:31], v[14:15]
	v_mov_b32_e32 v53, 0
	v_pk_mul_f32 v[54:55], v[32:33], v[12:13]
	v_cvt_pk_fp8_f32 v53, v14, v15
	v_cvt_pk_bf16_f32 v12, v50, v51
	v_cvt_pk_fp8_f32 v52, v16, v17 op_sel:[0,0,1]
	v_cvt_pk_bf16_f32 v13, v16, v17
	v_cvt_pk_bf16_f32 v14, v14, v15
	v_cvt_pk_bf16_f32 v15, v54, v55
	v_add_u32_e32 v16, s60, v163
	v_pk_mul_f32 v[4:5], v[0:1], v[4:5] op_sel_hi:[0,1]
	ds_write_b128 v16, v[12:15]
	v_pk_mul_f32 v[10:11], v[0:1], v[10:11] op_sel_hi:[0,1]
	v_pk_mul_f32 v[12:13], v[20:21], v[4:5]
	v_pk_mul_f32 v[4:5], v[0:1], v[8:9] op_sel_hi:[0,1]
	v_pk_mul_f32 v[10:11], v[18:19], v[10:11]
	v_pk_mul_f32 v[8:9], v[22:23], v[4:5]
	v_mov_b32_e32 v14, 0
	v_mov_b32_e32 v15, 0
	v_cvt_pk_fp8_f32 v14, v10, v11
	v_cvt_pk_fp8_f32 v15, v8, v9
	v_pk_mul_f32 v[4:5], v[0:1], v[6:7] op_sel_hi:[0,1]
	v_pk_mul_f32 v[16:17], v[24:25], v[4:5]
	v_cvt_pk_fp8_f32 v83, v84, v85 op_sel:[0,0,1]
	v_cvt_pk_fp8_f32 v61, v62, v63 op_sel:[0,0,1]
	v_cvt_pk_fp8_f32 v53, v54, v55 op_sel:[0,0,1]
	v_cvt_pk_fp8_f32 v14, v12, v13 op_sel:[0,0,1]
	v_cvt_pk_fp8_f32 v15, v16, v17 op_sel:[0,0,1]
	global_store_dwordx2 v[2:3], v[82:83], off
	global_store_dwordx2 v[2:3], v[60:61], off offset:512
	global_store_dwordx2 v[2:3], v[52:53], off offset:1024
	v_cvt_pk_bf16_f32 v4, v10, v11
	v_cvt_pk_bf16_f32 v5, v12, v13
	v_cvt_pk_bf16_f32 v6, v8, v9
	v_cvt_pk_bf16_f32 v7, v16, v17
	global_store_dwordx2 v[2:3], v[14:15], off offset:1536
	v_add_u32_e32 v0, s60, v164
	v_mov_b32_e32 v2, 0
	ds_write_b128 v0, v[4:7]
	v_mov_b64_e32 v[50:51], v[78:79]
	v_mov_b32_e32 v3, v2
	v_mov_b32_e32 v4, v2
	v_mov_b32_e32 v5, v2
	v_mov_b32_e32 v6, v2
	v_mov_b32_e32 v7, v2
	v_mov_b32_e32 v8, v2
	v_mov_b32_e32 v9, v2
	v_mov_b32_e32 v10, v2
	v_mov_b32_e32 v11, v2
	v_mov_b32_e32 v12, v2
	v_mov_b32_e32 v13, v2
	v_mov_b32_e32 v14, v2
	v_mov_b32_e32 v15, v2
	v_mov_b32_e32 v16, v2
	v_mov_b32_e32 v17, v2
	s_waitcnt lgkmcnt(0)
	s_barrier
